# conformer conv post-processing: xor-16/xor-32 reduction steps via v_permlane16/32_swap on two copies instead of ds_bpermute + lgkmcnt(0)
# speedup vs baseline: 1.0041x; 1.0041x over previous
.LBB0_2165:
	ds_read_u16 v29, v22
	ds_read_u16 v30, v22 offset:1024
	ds_read_u16 v31, v22 offset:2048
	ds_read_u16 v32, v22 offset:3072
	ds_read_u16 v33, v22 offset:4096
	ds_read_u16 v34, v22 offset:5120
	ds_read_u16 v35, v22 offset:6144
	ds_read_u16 v36, v22 offset:7168
	s_waitcnt lgkmcnt(7)
	v_lshlrev_b32_e32 v29, 16, v29
	v_fma_f32 v29, v51, v29, v52
	s_waitcnt lgkmcnt(6)
	v_lshlrev_b32_e32 v30, 16, v30
	v_fmac_f32_e32 v29, v54, v30
	v_fma_f32 v30, v51, v30, v52
	s_waitcnt lgkmcnt(5)
	v_lshlrev_b32_e32 v31, 16, v31
	v_fmac_f32_e32 v29, v55, v31
	v_fmac_f32_e32 v30, v54, v31
	v_fma_f32 v31, v51, v31, v52
	s_waitcnt lgkmcnt(4)
	v_lshlrev_b32_e32 v32, 16, v32
	ds_read_u16 v37, v22 offset:8192
	ds_read_u16 v38, v22 offset:9216
	ds_read_u16 v39, v22 offset:10240
	ds_read_u16 v40, v22 offset:11264
	ds_read_u16 v41, v22 offset:12288
	ds_read_u16 v42, v22 offset:13312
	ds_read_u16 v43, v22 offset:14336
	ds_read_u16 v44, v22 offset:15360
	v_fmac_f32_e32 v29, v56, v32
	v_fmac_f32_e32 v30, v55, v32
	v_fmac_f32_e32 v31, v54, v32
	v_fma_f32 v32, v51, v32, v52
	s_waitcnt lgkmcnt(11)
	v_lshlrev_b32_e32 v33, 16, v33
	v_fmac_f32_e32 v29, v57, v33
	v_fmac_f32_e32 v30, v56, v33
	v_fmac_f32_e32 v31, v55, v33
	v_fmac_f32_e32 v32, v54, v33
	v_fma_f32 v33, v51, v33, v52
	s_waitcnt lgkmcnt(10)
	v_lshlrev_b32_e32 v34, 16, v34
	v_fmac_f32_e32 v29, v58, v34
	v_fmac_f32_e32 v30, v57, v34
	v_fmac_f32_e32 v31, v56, v34
	v_fmac_f32_e32 v32, v55, v34
	v_fmac_f32_e32 v33, v54, v34
	v_fma_f32 v34, v51, v34, v52
	s_waitcnt lgkmcnt(9)
	v_lshlrev_b32_e32 v35, 16, v35
	v_fmac_f32_e32 v29, v59, v35
	v_fmac_f32_e32 v30, v58, v35
	v_fmac_f32_e32 v31, v57, v35
	v_fmac_f32_e32 v32, v56, v35
	v_fmac_f32_e32 v33, v55, v35
	v_fmac_f32_e32 v34, v54, v35
	v_fma_f32 v35, v51, v35, v52
	s_waitcnt lgkmcnt(8)
	v_lshlrev_b32_e32 v36, 16, v36
	v_fmac_f32_e32 v29, v60, v36
	v_fmac_f32_e32 v30, v59, v36
	v_fmac_f32_e32 v31, v58, v36
	v_fmac_f32_e32 v32, v57, v36
	v_fmac_f32_e32 v33, v56, v36
	v_fmac_f32_e32 v34, v55, v36
	v_fmac_f32_e32 v35, v54, v36
	v_fma_f32 v36, v51, v36, v52
	s_waitcnt lgkmcnt(7)
	v_lshlrev_b32_e32 v37, 16, v37
	v_fmac_f32_e32 v29, v61, v37
	v_fmac_f32_e32 v30, v60, v37
	v_fmac_f32_e32 v31, v59, v37
	v_fmac_f32_e32 v32, v58, v37
	v_fmac_f32_e32 v33, v57, v37
	v_fmac_f32_e32 v34, v56, v37
	v_fmac_f32_e32 v35, v55, v37
	v_fmac_f32_e32 v36, v54, v37
	v_fma_f32 v37, v51, v37, v52
	s_waitcnt lgkmcnt(6)
	v_lshlrev_b32_e32 v38, 16, v38
	v_fmac_f32_e32 v29, v62, v38
	v_fmac_f32_e32 v30, v61, v38
	v_fmac_f32_e32 v31, v60, v38
	v_fmac_f32_e32 v32, v59, v38
	v_fmac_f32_e32 v33, v58, v38
	v_fmac_f32_e32 v34, v57, v38
	v_fmac_f32_e32 v35, v56, v38
	v_fmac_f32_e32 v36, v55, v38
	v_fmac_f32_e32 v37, v54, v38
	v_fma_f32 v38, v51, v38, v52
	s_waitcnt lgkmcnt(5)
	v_lshlrev_b32_e32 v39, 16, v39
	v_fmac_f32_e32 v29, v63, v39
	v_fmac_f32_e32 v30, v62, v39
	v_fmac_f32_e32 v31, v61, v39
	v_fmac_f32_e32 v32, v60, v39
	v_fmac_f32_e32 v33, v59, v39
	v_fmac_f32_e32 v34, v58, v39
	v_fmac_f32_e32 v35, v57, v39
	v_fmac_f32_e32 v36, v56, v39
	v_fmac_f32_e32 v37, v55, v39
	v_fmac_f32_e32 v38, v54, v39
	v_fma_f32 v39, v51, v39, v52
	s_waitcnt lgkmcnt(4)
	v_lshlrev_b32_e32 v40, 16, v40
	ds_read_u16 v45, v22 offset:16384
	v_fmac_f32_e32 v29, v64, v40
	v_fmac_f32_e32 v30, v63, v40
	v_fmac_f32_e32 v31, v62, v40
	v_fmac_f32_e32 v32, v61, v40
	v_fmac_f32_e32 v33, v60, v40
	v_fmac_f32_e32 v34, v59, v40
	v_fmac_f32_e32 v35, v58, v40
	v_fmac_f32_e32 v36, v57, v40
	v_fmac_f32_e32 v37, v56, v40
	v_fmac_f32_e32 v38, v55, v40
	v_fmac_f32_e32 v39, v54, v40
	v_fma_f32 v40, v51, v40, v52
	s_waitcnt lgkmcnt(4)
	v_lshlrev_b32_e32 v41, 16, v41
	v_fmac_f32_e32 v29, v65, v41
	v_fmac_f32_e32 v30, v64, v41
	v_fmac_f32_e32 v31, v63, v41
	v_fmac_f32_e32 v32, v62, v41
	v_fmac_f32_e32 v33, v61, v41
	v_fmac_f32_e32 v34, v60, v41
	v_fmac_f32_e32 v35, v59, v41
	v_fmac_f32_e32 v36, v58, v41
	v_fmac_f32_e32 v37, v57, v41
	v_fmac_f32_e32 v38, v56, v41
	v_fmac_f32_e32 v39, v55, v41
	v_fmac_f32_e32 v40, v54, v41
	v_fma_f32 v41, v51, v41, v52
	s_waitcnt lgkmcnt(3)
	v_lshlrev_b32_e32 v42, 16, v42
	v_fmac_f32_e32 v29, v66, v42
	v_fmac_f32_e32 v30, v65, v42
	v_fmac_f32_e32 v31, v64, v42
	v_fmac_f32_e32 v32, v63, v42
	v_fmac_f32_e32 v33, v62, v42
	v_fmac_f32_e32 v34, v61, v42
	v_fmac_f32_e32 v35, v60, v42
	v_fmac_f32_e32 v36, v59, v42
	v_fmac_f32_e32 v37, v58, v42
	v_fmac_f32_e32 v38, v57, v42
	v_fmac_f32_e32 v39, v56, v42
	v_fmac_f32_e32 v40, v55, v42
	v_fmac_f32_e32 v41, v54, v42
	v_fma_f32 v42, v51, v42, v52
	s_waitcnt lgkmcnt(2)
	v_lshlrev_b32_e32 v43, 16, v43
	v_fmac_f32_e32 v29, v67, v43
	v_fmac_f32_e32 v30, v66, v43
	v_fmac_f32_e32 v31, v65, v43
	v_fmac_f32_e32 v32, v64, v43
	v_fmac_f32_e32 v33, v63, v43
	v_fmac_f32_e32 v34, v62, v43
	v_fmac_f32_e32 v35, v61, v43
	v_fmac_f32_e32 v36, v60, v43
	v_fmac_f32_e32 v37, v59, v43
	v_fmac_f32_e32 v38, v58, v43
	v_fmac_f32_e32 v39, v57, v43
	v_fmac_f32_e32 v40, v56, v43
	v_fmac_f32_e32 v41, v55, v43
	v_fmac_f32_e32 v42, v54, v43
	v_fma_f32 v43, v51, v43, v52
	s_waitcnt lgkmcnt(1)
	v_lshlrev_b32_e32 v44, 16, v44
	v_fmac_f32_e32 v29, v68, v44
	v_fmac_f32_e32 v30, v67, v44
	v_fmac_f32_e32 v31, v66, v44
	v_fmac_f32_e32 v32, v65, v44
	v_fmac_f32_e32 v33, v64, v44
	v_fmac_f32_e32 v34, v63, v44
	v_fmac_f32_e32 v35, v62, v44
	v_fmac_f32_e32 v36, v61, v44
	v_fmac_f32_e32 v37, v60, v44
	v_fmac_f32_e32 v38, v59, v44
	v_fmac_f32_e32 v39, v58, v44
	v_fmac_f32_e32 v40, v57, v44
	v_fmac_f32_e32 v41, v56, v44
	v_fmac_f32_e32 v42, v55, v44
	v_fmac_f32_e32 v43, v54, v44
	v_fma_f32 v44, v51, v44, v52
	s_waitcnt lgkmcnt(0)
	v_lshlrev_b32_e32 v45, 16, v45
	v_fmac_f32_e32 v29, v69, v45
	v_fmac_f32_e32 v30, v68, v45
	v_fmac_f32_e32 v31, v67, v45
	v_fmac_f32_e32 v32, v66, v45
	v_fmac_f32_e32 v33, v65, v45
	v_fmac_f32_e32 v34, v64, v45
	v_fmac_f32_e32 v35, v63, v45
	v_fmac_f32_e32 v36, v62, v45
	v_fmac_f32_e32 v37, v61, v45
	v_fmac_f32_e32 v38, v60, v45
	v_fmac_f32_e32 v39, v59, v45
	v_fmac_f32_e32 v40, v58, v45
	v_fmac_f32_e32 v41, v57, v45
	v_fmac_f32_e32 v42, v56, v45
	v_fmac_f32_e32 v43, v55, v45
	v_fmac_f32_e32 v44, v54, v45
	ds_read_u16 v100, v22 offset:17408
	ds_read_u16 v101, v22 offset:18432
	ds_read_u16 v102, v22 offset:19456
	ds_read_u16 v103, v22 offset:20480
	ds_read_u16 v104, v22 offset:21504
	ds_read_u16 v105, v22 offset:22528
	ds_read_u16 v106, v22 offset:23552
	ds_read_u16 v107, v22 offset:24576
	s_waitcnt lgkmcnt(7)
	v_lshlrev_b32_e32 v45, 16, v100
	ds_read_u16 v100, v22 offset:25600
	v_fmac_f32_e32 v29, v70, v45
	v_fmac_f32_e32 v30, v69, v45
	v_fmac_f32_e32 v31, v68, v45
	v_fmac_f32_e32 v32, v67, v45
	v_fmac_f32_e32 v33, v66, v45
	v_fmac_f32_e32 v34, v65, v45
	v_fmac_f32_e32 v35, v64, v45
	v_fmac_f32_e32 v36, v63, v45
	v_fmac_f32_e32 v37, v62, v45
	v_fmac_f32_e32 v38, v61, v45
	v_fmac_f32_e32 v39, v60, v45
	v_fmac_f32_e32 v40, v59, v45
	v_fmac_f32_e32 v41, v58, v45
	v_fmac_f32_e32 v42, v57, v45
	v_fmac_f32_e32 v43, v56, v45
	v_fmac_f32_e32 v44, v55, v45
	s_waitcnt lgkmcnt(7)
	v_lshlrev_b32_e32 v45, 16, v101
	ds_read_u16 v101, v22 offset:26624
	v_fmac_f32_e32 v29, v71, v45
	v_fmac_f32_e32 v30, v70, v45
	v_fmac_f32_e32 v31, v69, v45
	v_fmac_f32_e32 v32, v68, v45
	v_fmac_f32_e32 v33, v67, v45
	v_fmac_f32_e32 v34, v66, v45
	v_fmac_f32_e32 v35, v65, v45
	v_fmac_f32_e32 v36, v64, v45
	v_fmac_f32_e32 v37, v63, v45
	v_fmac_f32_e32 v38, v62, v45
	v_fmac_f32_e32 v39, v61, v45
	v_fmac_f32_e32 v40, v60, v45
	v_fmac_f32_e32 v41, v59, v45
	v_fmac_f32_e32 v42, v58, v45
	v_fmac_f32_e32 v43, v57, v45
	v_fmac_f32_e32 v44, v56, v45
	s_waitcnt lgkmcnt(7)
	v_lshlrev_b32_e32 v45, 16, v102
	ds_read_u16 v102, v22 offset:27648
	v_fmac_f32_e32 v29, v72, v45
	v_fmac_f32_e32 v30, v71, v45
	v_fmac_f32_e32 v31, v70, v45
	v_fmac_f32_e32 v32, v69, v45
	v_fmac_f32_e32 v33, v68, v45
	v_fmac_f32_e32 v34, v67, v45
	v_fmac_f32_e32 v35, v66, v45
	v_fmac_f32_e32 v36, v65, v45
	v_fmac_f32_e32 v37, v64, v45
	v_fmac_f32_e32 v38, v63, v45
	v_fmac_f32_e32 v39, v62, v45
	v_fmac_f32_e32 v40, v61, v45
	v_fmac_f32_e32 v41, v60, v45
	v_fmac_f32_e32 v42, v59, v45
	v_fmac_f32_e32 v43, v58, v45
	v_fmac_f32_e32 v44, v57, v45
	s_waitcnt lgkmcnt(7)
	v_lshlrev_b32_e32 v45, 16, v103
	ds_read_u16 v103, v22 offset:28672
	v_fmac_f32_e32 v29, v73, v45
	v_fmac_f32_e32 v30, v72, v45
	v_fmac_f32_e32 v31, v71, v45
	v_fmac_f32_e32 v32, v70, v45
	v_fmac_f32_e32 v33, v69, v45
	v_fmac_f32_e32 v34, v68, v45
	v_fmac_f32_e32 v35, v67, v45
	v_fmac_f32_e32 v36, v66, v45
	v_fmac_f32_e32 v37, v65, v45
	v_fmac_f32_e32 v38, v64, v45
	v_fmac_f32_e32 v39, v63, v45
	v_fmac_f32_e32 v40, v62, v45
	v_fmac_f32_e32 v41, v61, v45
	v_fmac_f32_e32 v42, v60, v45
	v_fmac_f32_e32 v43, v59, v45
	v_fmac_f32_e32 v44, v58, v45
	s_waitcnt lgkmcnt(7)
	v_lshlrev_b32_e32 v45, 16, v104
	ds_read_u16 v104, v22 offset:29696
	v_fmac_f32_e32 v29, v74, v45
	v_fmac_f32_e32 v30, v73, v45
	v_fmac_f32_e32 v31, v72, v45
	v_fmac_f32_e32 v32, v71, v45
	v_fmac_f32_e32 v33, v70, v45
	v_fmac_f32_e32 v34, v69, v45
	v_fmac_f32_e32 v35, v68, v45
	v_fmac_f32_e32 v36, v67, v45
	v_fmac_f32_e32 v37, v66, v45
	v_fmac_f32_e32 v38, v65, v45
	v_fmac_f32_e32 v39, v64, v45
	v_fmac_f32_e32 v40, v63, v45
	v_fmac_f32_e32 v41, v62, v45
	v_fmac_f32_e32 v42, v61, v45
	v_fmac_f32_e32 v43, v60, v45
	v_fmac_f32_e32 v44, v59, v45
	s_waitcnt lgkmcnt(7)
	v_lshlrev_b32_e32 v45, 16, v105
	ds_read_u16 v105, v22 offset:30720
	v_fmac_f32_e32 v29, v75, v45
	v_fmac_f32_e32 v30, v74, v45
	v_fmac_f32_e32 v31, v73, v45
	v_fmac_f32_e32 v32, v72, v45
	v_fmac_f32_e32 v33, v71, v45
	v_fmac_f32_e32 v34, v70, v45
	v_fmac_f32_e32 v35, v69, v45
	v_fmac_f32_e32 v36, v68, v45
	v_fmac_f32_e32 v37, v67, v45
	v_fmac_f32_e32 v38, v66, v45
	v_fmac_f32_e32 v39, v65, v45
	v_fmac_f32_e32 v40, v64, v45
	v_fmac_f32_e32 v41, v63, v45
	v_fmac_f32_e32 v42, v62, v45
	v_fmac_f32_e32 v43, v61, v45
	v_fmac_f32_e32 v44, v60, v45
	s_waitcnt lgkmcnt(7)
	v_lshlrev_b32_e32 v45, 16, v106
	ds_read_u16 v106, v22 offset:31744
	v_fmac_f32_e32 v29, v76, v45
	v_fmac_f32_e32 v30, v75, v45
	v_fmac_f32_e32 v31, v74, v45
	v_fmac_f32_e32 v32, v73, v45
	v_fmac_f32_e32 v33, v72, v45
	v_fmac_f32_e32 v34, v71, v45
	v_fmac_f32_e32 v35, v70, v45
	v_fmac_f32_e32 v36, v69, v45
	v_fmac_f32_e32 v37, v68, v45
	v_fmac_f32_e32 v38, v67, v45
	v_fmac_f32_e32 v39, v66, v45
	v_fmac_f32_e32 v40, v65, v45
	v_fmac_f32_e32 v41, v64, v45
	v_fmac_f32_e32 v42, v63, v45
	v_fmac_f32_e32 v43, v62, v45
	v_fmac_f32_e32 v44, v61, v45
	s_waitcnt lgkmcnt(7)
	v_lshlrev_b32_e32 v45, 16, v107
	ds_read_u16 v107, v22 offset:32768
	v_fmac_f32_e32 v29, v77, v45
	v_fmac_f32_e32 v30, v76, v45
	v_fmac_f32_e32 v31, v75, v45
	v_fmac_f32_e32 v32, v74, v45
	v_fmac_f32_e32 v33, v73, v45
	v_fmac_f32_e32 v34, v72, v45
	v_fmac_f32_e32 v35, v71, v45
	v_fmac_f32_e32 v36, v70, v45
	v_fmac_f32_e32 v37, v69, v45
	v_fmac_f32_e32 v38, v68, v45
	v_fmac_f32_e32 v39, v67, v45
	v_fmac_f32_e32 v40, v66, v45
	v_fmac_f32_e32 v41, v65, v45
	v_fmac_f32_e32 v42, v64, v45
	v_fmac_f32_e32 v43, v63, v45
	v_fmac_f32_e32 v44, v62, v45
	s_waitcnt lgkmcnt(7)
	v_lshlrev_b32_e32 v45, 16, v100
	ds_read_u16 v100, v22 offset:33792
	v_fmac_f32_e32 v29, v78, v45
	v_fmac_f32_e32 v30, v77, v45
	v_fmac_f32_e32 v31, v76, v45
	v_fmac_f32_e32 v32, v75, v45
	v_fmac_f32_e32 v33, v74, v45
	v_fmac_f32_e32 v34, v73, v45
	v_fmac_f32_e32 v35, v72, v45
	v_fmac_f32_e32 v36, v71, v45
	v_fmac_f32_e32 v37, v70, v45
	v_fmac_f32_e32 v38, v69, v45
	v_fmac_f32_e32 v39, v68, v45
	v_fmac_f32_e32 v40, v67, v45
	v_fmac_f32_e32 v41, v66, v45
	v_fmac_f32_e32 v42, v65, v45
	v_fmac_f32_e32 v43, v64, v45
	v_fmac_f32_e32 v44, v63, v45
	s_waitcnt lgkmcnt(7)
	v_lshlrev_b32_e32 v45, 16, v101
	ds_read_u16 v101, v22 offset:34816
	v_fmac_f32_e32 v29, v79, v45
	v_fmac_f32_e32 v30, v78, v45
	v_fmac_f32_e32 v31, v77, v45
	v_fmac_f32_e32 v32, v76, v45
	v_fmac_f32_e32 v33, v75, v45
	v_fmac_f32_e32 v34, v74, v45
	v_fmac_f32_e32 v35, v73, v45
	v_fmac_f32_e32 v36, v72, v45
	v_fmac_f32_e32 v37, v71, v45
	v_fmac_f32_e32 v38, v70, v45
	v_fmac_f32_e32 v39, v69, v45
	v_fmac_f32_e32 v40, v68, v45
	v_fmac_f32_e32 v41, v67, v45
	v_fmac_f32_e32 v42, v66, v45
	v_fmac_f32_e32 v43, v65, v45
	v_fmac_f32_e32 v44, v64, v45
	s_waitcnt lgkmcnt(7)
	v_lshlrev_b32_e32 v45, 16, v102
	ds_read_u16 v102, v22 offset:35840
	v_fmac_f32_e32 v29, v80, v45
	v_fmac_f32_e32 v30, v79, v45
	v_fmac_f32_e32 v31, v78, v45
	v_fmac_f32_e32 v32, v77, v45
	v_fmac_f32_e32 v33, v76, v45
	v_fmac_f32_e32 v34, v75, v45
	v_fmac_f32_e32 v35, v74, v45
	v_fmac_f32_e32 v36, v73, v45
	v_fmac_f32_e32 v37, v72, v45
	v_fmac_f32_e32 v38, v71, v45
	v_fmac_f32_e32 v39, v70, v45
	v_fmac_f32_e32 v40, v69, v45
	v_fmac_f32_e32 v41, v68, v45
	v_fmac_f32_e32 v42, v67, v45
	v_fmac_f32_e32 v43, v66, v45
	v_fmac_f32_e32 v44, v65, v45
	s_waitcnt lgkmcnt(7)
	v_lshlrev_b32_e32 v45, 16, v103
	ds_read_u16 v103, v22 offset:36864
	v_fmac_f32_e32 v29, v81, v45
	v_fmac_f32_e32 v30, v80, v45
	v_fmac_f32_e32 v31, v79, v45
	v_fmac_f32_e32 v32, v78, v45
	v_fmac_f32_e32 v33, v77, v45
	v_fmac_f32_e32 v34, v76, v45
	v_fmac_f32_e32 v35, v75, v45
	v_fmac_f32_e32 v36, v74, v45
	v_fmac_f32_e32 v37, v73, v45
	v_fmac_f32_e32 v38, v72, v45
	v_fmac_f32_e32 v39, v71, v45
	v_fmac_f32_e32 v40, v70, v45
	v_fmac_f32_e32 v41, v69, v45
	v_fmac_f32_e32 v42, v68, v45
	v_fmac_f32_e32 v43, v67, v45
	v_fmac_f32_e32 v44, v66, v45
	s_waitcnt lgkmcnt(7)
	v_lshlrev_b32_e32 v45, 16, v104
	ds_read_u16 v104, v22 offset:37888
	v_fmac_f32_e32 v29, v82, v45
	v_fmac_f32_e32 v30, v81, v45
	v_fmac_f32_e32 v31, v80, v45
	v_fmac_f32_e32 v32, v79, v45
	v_fmac_f32_e32 v33, v78, v45
	v_fmac_f32_e32 v34, v77, v45
	v_fmac_f32_e32 v35, v76, v45
	v_fmac_f32_e32 v36, v75, v45
	v_fmac_f32_e32 v37, v74, v45
	v_fmac_f32_e32 v38, v73, v45
	v_fmac_f32_e32 v39, v72, v45
	v_fmac_f32_e32 v40, v71, v45
	v_fmac_f32_e32 v41, v70, v45
	v_fmac_f32_e32 v42, v69, v45
	v_fmac_f32_e32 v43, v68, v45
	v_fmac_f32_e32 v44, v67, v45
	s_waitcnt lgkmcnt(7)
	v_lshlrev_b32_e32 v45, 16, v105
	ds_read_u16 v105, v22 offset:38912
	v_fmac_f32_e32 v29, v83, v45
	v_fmac_f32_e32 v30, v82, v45
	v_fmac_f32_e32 v31, v81, v45
	v_fmac_f32_e32 v32, v80, v45
	v_fmac_f32_e32 v33, v79, v45
	v_fmac_f32_e32 v34, v78, v45
	v_fmac_f32_e32 v35, v77, v45
	v_fmac_f32_e32 v36, v76, v45
	v_fmac_f32_e32 v37, v75, v45
	v_fmac_f32_e32 v38, v74, v45
	v_fmac_f32_e32 v39, v73, v45
	v_fmac_f32_e32 v40, v72, v45
	v_fmac_f32_e32 v41, v71, v45
	v_fmac_f32_e32 v42, v70, v45
	v_fmac_f32_e32 v43, v69, v45
	v_fmac_f32_e32 v44, v68, v45
	s_waitcnt lgkmcnt(7)
	v_lshlrev_b32_e32 v45, 16, v106
	ds_read_u16 v106, v22 offset:39936
	v_fmac_f32_e32 v30, v83, v45
	v_fmac_f32_e32 v31, v82, v45
	v_fmac_f32_e32 v32, v81, v45
	v_fmac_f32_e32 v33, v80, v45
	v_fmac_f32_e32 v34, v79, v45
	v_fmac_f32_e32 v35, v78, v45
	v_fmac_f32_e32 v36, v77, v45
	v_fmac_f32_e32 v37, v76, v45
	v_fmac_f32_e32 v38, v75, v45
	v_fmac_f32_e32 v39, v74, v45
	v_fmac_f32_e32 v40, v73, v45
	v_fmac_f32_e32 v41, v72, v45
	v_fmac_f32_e32 v42, v71, v45
	v_fmac_f32_e32 v43, v70, v45
	v_fmac_f32_e32 v44, v69, v45
	s_waitcnt lgkmcnt(7)
	v_lshlrev_b32_e32 v45, 16, v107
	ds_read_u16 v107, v22 offset:40960
	v_fmac_f32_e32 v31, v83, v45
	v_fmac_f32_e32 v32, v82, v45
	v_fmac_f32_e32 v33, v81, v45
	v_fmac_f32_e32 v34, v80, v45
	v_fmac_f32_e32 v35, v79, v45
	v_fmac_f32_e32 v36, v78, v45
	v_fmac_f32_e32 v37, v77, v45
	v_fmac_f32_e32 v38, v76, v45
	v_fmac_f32_e32 v39, v75, v45
	v_fmac_f32_e32 v40, v74, v45
	v_fmac_f32_e32 v41, v73, v45
	v_fmac_f32_e32 v42, v72, v45
	v_fmac_f32_e32 v43, v71, v45
	v_fmac_f32_e32 v44, v70, v45
	s_waitcnt lgkmcnt(7)
	v_lshlrev_b32_e32 v45, 16, v100
	ds_read_u16 v100, v22 offset:41984
	v_fmac_f32_e32 v32, v83, v45
	v_fmac_f32_e32 v33, v82, v45
	v_fmac_f32_e32 v34, v81, v45
	v_fmac_f32_e32 v35, v80, v45
	v_fmac_f32_e32 v36, v79, v45
	v_fmac_f32_e32 v37, v78, v45
	v_fmac_f32_e32 v38, v77, v45
	v_fmac_f32_e32 v39, v76, v45
	v_fmac_f32_e32 v40, v75, v45
	v_fmac_f32_e32 v41, v74, v45
	v_fmac_f32_e32 v42, v73, v45
	v_fmac_f32_e32 v43, v72, v45
	v_fmac_f32_e32 v44, v71, v45
	s_waitcnt lgkmcnt(7)
	v_lshlrev_b32_e32 v45, 16, v101
	ds_read_u16 v101, v22 offset:43008
	v_fmac_f32_e32 v33, v83, v45
	v_fmac_f32_e32 v34, v82, v45
	v_fmac_f32_e32 v35, v81, v45
	v_fmac_f32_e32 v36, v80, v45
	v_fmac_f32_e32 v37, v79, v45
	v_fmac_f32_e32 v38, v78, v45
	v_fmac_f32_e32 v39, v77, v45
	v_fmac_f32_e32 v40, v76, v45
	v_fmac_f32_e32 v41, v75, v45
	v_fmac_f32_e32 v42, v74, v45
	v_fmac_f32_e32 v43, v73, v45
	v_fmac_f32_e32 v44, v72, v45
	s_waitcnt lgkmcnt(7)
	v_lshlrev_b32_e32 v45, 16, v102
	ds_read_u16 v102, v22 offset:44032
	v_fmac_f32_e32 v34, v83, v45
	v_fmac_f32_e32 v35, v82, v45
	v_fmac_f32_e32 v36, v81, v45
	v_fmac_f32_e32 v37, v80, v45
	v_fmac_f32_e32 v38, v79, v45
	v_fmac_f32_e32 v39, v78, v45
	v_fmac_f32_e32 v40, v77, v45
	v_fmac_f32_e32 v41, v76, v45
	v_fmac_f32_e32 v42, v75, v45
	v_fmac_f32_e32 v43, v74, v45
	v_fmac_f32_e32 v44, v73, v45
	s_waitcnt lgkmcnt(7)
	v_lshlrev_b32_e32 v45, 16, v103
	ds_read_u16 v103, v22 offset:45056
	v_fmac_f32_e32 v35, v83, v45
	v_fmac_f32_e32 v36, v82, v45
	v_fmac_f32_e32 v37, v81, v45
	v_fmac_f32_e32 v38, v80, v45
	v_fmac_f32_e32 v39, v79, v45
	v_fmac_f32_e32 v40, v78, v45
	v_fmac_f32_e32 v41, v77, v45
	v_fmac_f32_e32 v42, v76, v45
	v_fmac_f32_e32 v43, v75, v45
	v_fmac_f32_e32 v44, v74, v45
	s_waitcnt lgkmcnt(7)
	v_lshlrev_b32_e32 v45, 16, v104
	ds_read_u16 v104, v22 offset:46080
	v_fmac_f32_e32 v36, v83, v45
	v_fmac_f32_e32 v37, v82, v45
	v_fmac_f32_e32 v38, v81, v45
	v_fmac_f32_e32 v39, v80, v45
	v_fmac_f32_e32 v40, v79, v45
	v_fmac_f32_e32 v41, v78, v45
	v_fmac_f32_e32 v42, v77, v45
	v_fmac_f32_e32 v43, v76, v45
	v_fmac_f32_e32 v44, v75, v45
	s_waitcnt lgkmcnt(7)
	v_lshlrev_b32_e32 v45, 16, v105
	v_fmac_f32_e32 v37, v83, v45
	v_fmac_f32_e32 v38, v82, v45
	v_fmac_f32_e32 v39, v81, v45
	v_fmac_f32_e32 v40, v80, v45
	v_fmac_f32_e32 v41, v79, v45
	v_fmac_f32_e32 v42, v78, v45
	v_fmac_f32_e32 v43, v77, v45
	v_fmac_f32_e32 v44, v76, v45
	s_waitcnt lgkmcnt(6)
	v_lshlrev_b32_e32 v45, 16, v106
	v_fmac_f32_e32 v38, v83, v45
	v_fmac_f32_e32 v39, v82, v45
	v_fmac_f32_e32 v40, v81, v45
	v_fmac_f32_e32 v41, v80, v45
	v_fmac_f32_e32 v42, v79, v45
	v_fmac_f32_e32 v43, v78, v45
	v_fmac_f32_e32 v44, v77, v45
	s_waitcnt lgkmcnt(5)
	v_lshlrev_b32_e32 v45, 16, v107
	v_fmac_f32_e32 v39, v83, v45
	v_fmac_f32_e32 v40, v82, v45
	v_fmac_f32_e32 v41, v81, v45
	v_fmac_f32_e32 v42, v80, v45
	v_fmac_f32_e32 v43, v79, v45
	v_fmac_f32_e32 v44, v78, v45
	s_waitcnt lgkmcnt(4)
	v_lshlrev_b32_e32 v45, 16, v100
	v_fmac_f32_e32 v40, v83, v45
	v_fmac_f32_e32 v41, v82, v45
	v_fmac_f32_e32 v42, v81, v45
	v_fmac_f32_e32 v43, v80, v45
	v_fmac_f32_e32 v44, v79, v45
	s_waitcnt lgkmcnt(3)
	v_lshlrev_b32_e32 v45, 16, v101
	v_fmac_f32_e32 v41, v83, v45
	v_fmac_f32_e32 v42, v82, v45
	v_fmac_f32_e32 v43, v81, v45
	v_fmac_f32_e32 v44, v80, v45
	s_waitcnt lgkmcnt(2)
	v_lshlrev_b32_e32 v45, 16, v102
	v_fmac_f32_e32 v42, v83, v45
	v_fmac_f32_e32 v43, v82, v45
	v_fmac_f32_e32 v44, v81, v45
	s_waitcnt lgkmcnt(1)
	v_lshlrev_b32_e32 v45, 16, v103
	v_fmac_f32_e32 v43, v83, v45
	v_fmac_f32_e32 v44, v82, v45
	s_waitcnt lgkmcnt(0)
	v_lshlrev_b32_e32 v45, 16, v104
	v_fmac_f32_e32 v44, v83, v45
	ds_write2st64_b32 v23, v29, v30 offset1:8
	ds_write2st64_b32 v23, v31, v32 offset0:16 offset1:24
	ds_write2st64_b32 v23, v33, v34 offset0:32 offset1:40
	ds_write2st64_b32 v23, v35, v36 offset0:48 offset1:56
	ds_write2st64_b32 v23, v37, v38 offset0:64 offset1:72
	ds_write2st64_b32 v23, v39, v40 offset0:80 offset1:88
	ds_write2st64_b32 v23, v41, v42 offset0:96 offset1:104
	ds_write2st64_b32 v23, v43, v44 offset0:112 offset1:120
	v_add_u32_e32 v29, s36, v24
	v_cmp_gt_i32_e32 vcc, 64, v29
	s_waitcnt lgkmcnt(0)
	s_barrier
	s_and_saveexec_b64 s[34:35], vcc
	s_cbranch_execz .LBB0_2167
	ds_read_b128 v[30:33], v27
	ds_read_b128 v[34:37], v27 offset:16
	s_waitcnt lgkmcnt(1)
	v_mov_b32_e32 v38, v31
	v_mov_b32_e32 v39, v32
	v_mov_b32_e32 v40, v30
	v_mov_b32_e32 v41, v33
	v_pk_add_f32 v[38:39], v[38:39], v[40:41]
	s_waitcnt lgkmcnt(0)
	v_mov_b32_e32 v40, v36
	v_mov_b32_e32 v41, v34
	v_mov_b32_e32 v42, v37
	v_mov_b32_e32 v43, v35
	v_pk_add_f32 v[40:41], v[40:41], v[42:43]
	v_add_f32_e32 v29, v38, v39
	v_add_f32_e32 v29, v29, v41
	v_add_f32_e32 v29, v40, v29
	v_and_b32_e32 v39, 64, v214
	v_xor_b32_e32 v38, 16, v214
	v_add_f32_dpp v29, v29, v29 quad_perm:[1,0,3,2] row_mask:0xf bank_mask:0xf bound_ctrl:1
	v_add_u32_e32 v39, 64, v39
	v_cmp_lt_i32_e32 vcc, v38, v39
	v_add_f32_dpp v29, v29, v29 quad_perm:[2,3,0,1] row_mask:0xf bank_mask:0xf bound_ctrl:1
	s_nop 0
	v_cndmask_b32_e32 v38, v214, v38, vcc
	v_add_f32_dpp v29, v29, v29 row_half_mirror row_mask:0xf bank_mask:0xf bound_ctrl:1
	v_lshlrev_b32_e32 v46, 2, v38
	s_nop 0
	v_add_f32_dpp v29, v29, v29 row_mirror row_mask:0xf bank_mask:0xf bound_ctrl:1
	v_mov_b32_e32 v38, v29
	v_mov_b32_e32 v108, v29
	s_nop 1
	v_permlane16_swap_b32_e32 v38, v108
	v_add_f32_e32 v29, v38, v108
	v_xor_b32_e32 v38, 32, v214
	v_cmp_lt_i32_e32 vcc, v38, v39
	s_nop 1
	v_cndmask_b32_e32 v38, v214, v38, vcc
	v_lshlrev_b32_e32 v47, 2, v38
	v_mov_b32_e32 v38, v29
	v_mov_b32_e32 v108, v29
	s_nop 1
	v_permlane32_swap_b32_e32 v38, v108
	v_add_f32_e32 v29, v38, v108
	v_fmamk_f32 v31, v29, 0xbb000000, v31
	v_fmamk_f32 v30, v29, 0xbb000000, v30
	v_fmamk_f32 v33, v29, 0xbb000000, v33
	v_fmac_f32_e32 v32, 0xbb000000, v29
	v_pk_mul_f32 v[38:39], v[32:33], v[32:33]
	v_pk_mul_f32 v[40:41], v[30:31], v[30:31]
	v_fmamk_f32 v35, v29, 0xbb000000, v35
	v_fmamk_f32 v34, v29, 0xbb000000, v34
	v_fmamk_f32 v37, v29, 0xbb000000, v37
	v_fmac_f32_e32 v36, 0xbb000000, v29
	v_pk_mov_b32 v[42:43], v[40:41], v[38:39] op_sel:[1,0]
	v_mov_b32_e32 v41, v39
	v_pk_add_f32 v[38:39], v[42:43], v[40:41]
	v_pk_mul_f32 v[40:41], v[36:37], v[36:37]
	v_pk_mul_f32 v[42:43], v[34:35], v[34:35]
	v_mov_b32_e32 v44, v40
	v_mov_b32_e32 v45, v42
	v_mov_b32_e32 v42, v41
	v_pk_add_f32 v[40:41], v[44:45], v[42:43]
	v_add_f32_e32 v29, v38, v39
	v_add_f32_e32 v29, v41, v29
	v_add_f32_e32 v29, v40, v29
	s_nop 1
	v_add_f32_dpp v29, v29, v29 quad_perm:[1,0,3,2] row_mask:0xf bank_mask:0xf bound_ctrl:1
	s_nop 1
	v_add_f32_dpp v29, v29, v29 quad_perm:[2,3,0,1] row_mask:0xf bank_mask:0xf bound_ctrl:1
	s_nop 1
	v_add_f32_dpp v29, v29, v29 row_half_mirror row_mask:0xf bank_mask:0xf bound_ctrl:1
	s_nop 1
	v_add_f32_dpp v29, v29, v29 row_mirror row_mask:0xf bank_mask:0xf bound_ctrl:1
	v_mov_b32_e32 v38, v29
	v_mov_b32_e32 v108, v29
	s_nop 1
	v_permlane16_swap_b32_e32 v38, v108
	v_add_f32_e32 v29, v38, v108
	v_mov_b32_e32 v38, v29
	v_mov_b32_e32 v108, v29
	s_nop 1
	v_permlane32_swap_b32_e32 v38, v108
	v_add_f32_e32 v29, v38, v108
	v_fmamk_f32 v29, v29, 0x3b000000, v1
	v_mul_f32_e32 v38, 0x4b800000, v29
	v_cmp_gt_f32_e32 vcc, s77, v29
	s_nop 1
	v_cndmask_b32_e32 v29, v29, v38, vcc
	v_rsq_f32_e32 v29, v29
	s_nop 0
	v_mul_f32_e32 v38, 0x45800000, v29
	v_cndmask_b32_e32 v38, v29, v38, vcc
	v_pk_mul_f32 v[30:31], v[30:31], v[38:39] op_sel_hi:[1,0]
	v_pk_mul_f32 v[34:35], v[34:35], v[38:39] op_sel_hi:[1,0]
	v_pk_fma_f32 v[30:31], v[6:7], v[30:31], v[14:15]
	v_pk_fma_f32 v[34:35], v[2:3], v[34:35], v[10:11]
	v_mul_f32_e32 v29, 0xbfb8aa3b, v30
	v_pk_mul_f32 v[32:33], v[32:33], v[38:39] op_sel_hi:[1,0]
	v_pk_mul_f32 v[36:37], v[36:37], v[38:39] op_sel_hi:[1,0]
	v_exp_f32_e32 v29, v29
	v_mul_f32_e32 v38, 0xbfb8aa3b, v34
	v_exp_f32_e32 v39, v38
	v_mul_f32_e32 v40, 0xbfb8aa3b, v35
	v_add_f32_e32 v29, 1.0, v29
	v_rcp_f32_e32 v38, v29
	v_add_f32_e32 v29, 1.0, v39
	v_mul_f32_e32 v39, 0xbfb8aa3b, v31
	v_exp_f32_e32 v39, v39
	v_exp_f32_e32 v41, v40
	v_pk_fma_f32 v[32:33], v[8:9], v[32:33], v[16:17]
	v_rcp_f32_e32 v40, v29
	v_add_f32_e32 v29, 1.0, v39
	v_pk_fma_f32 v[36:37], v[4:5], v[36:37], v[12:13]
	v_rcp_f32_e32 v39, v29
	v_add_f32_e32 v29, 1.0, v41
	v_mul_f32_e32 v41, 0xbfb8aa3b, v32
	v_exp_f32_e32 v42, v41
	v_mul_f32_e32 v41, 0xbfb8aa3b, v36
	v_exp_f32_e32 v43, v41
	v_rcp_f32_e32 v41, v29
	v_add_f32_e32 v29, 1.0, v42
	v_rcp_f32_e32 v42, v29
	v_add_f32_e32 v29, 1.0, v43
	v_mul_f32_e32 v43, 0xbfb8aa3b, v33
	v_exp_f32_e32 v43, v43
	v_mul_f32_e32 v44, 0xbfb8aa3b, v37
	v_exp_f32_e32 v45, v44
	v_rcp_f32_e32 v44, v29
	v_add_f32_e32 v29, 1.0, v43
	v_rcp_f32_e32 v43, v29
	v_add_f32_e32 v29, 1.0, v45
	v_rcp_f32_e32 v45, v29
	v_pk_mul_f32 v[30:31], v[30:31], v[38:39]
	v_pk_mul_f32 v[34:35], v[34:35], v[40:41]
	v_pk_mul_f32 v[32:33], v[32:33], v[42:43]
	v_cvt_pk_bf16_f32 v30, v30, v31
	v_cvt_pk_bf16_f32 v31, v32, v33
	v_cvt_pk_bf16_f32 v32, v34, v35
	v_add_u32_e32 v34, s36, v26
	v_ashrrev_i32_e32 v35, 31, v34
	v_pk_mul_f32 v[36:37], v[36:37], v[44:45]
	v_lshlrev_b64 v[34:35], 11, v[34:35]
	v_cvt_pk_bf16_f32 v33, v36, v37
	v_lshl_add_u64 v[34:35], v[18:19], 0, v[34:35]
	global_store_dwordx4 v[34:35], v[30:33], off offset:1024
.LBB0_2167:
	s_or_b64 exec, exec, s[34:35]
	v_add_u32_e32 v29, s36, v25
	v_cmp_gt_i32_e32 vcc, 64, v29
	s_and_saveexec_b64 s[34:35], vcc
	s_cbranch_execz .LBB0_2164
	ds_read_b128 v[30:33], v28
	ds_read_b128 v[34:37], v28 offset:16
	s_waitcnt lgkmcnt(1)
	v_mov_b32_e32 v38, v31
	v_mov_b32_e32 v39, v32
	v_mov_b32_e32 v40, v30
	v_mov_b32_e32 v41, v33
	v_pk_add_f32 v[38:39], v[38:39], v[40:41]
	s_waitcnt lgkmcnt(0)
	v_mov_b32_e32 v40, v36
	v_mov_b32_e32 v41, v34
	v_mov_b32_e32 v42, v37
	v_mov_b32_e32 v43, v35
	v_pk_add_f32 v[40:41], v[40:41], v[42:43]
	v_add_f32_e32 v29, v38, v39
	v_add_f32_e32 v29, v29, v41
	v_add_f32_e32 v29, v40, v29
	v_and_b32_e32 v39, 64, v214
	v_xor_b32_e32 v38, 16, v214
	v_add_f32_dpp v29, v29, v29 quad_perm:[1,0,3,2] row_mask:0xf bank_mask:0xf bound_ctrl:1
	v_add_u32_e32 v39, 64, v39
	v_cmp_lt_i32_e32 vcc, v38, v39
	v_add_f32_dpp v29, v29, v29 quad_perm:[2,3,0,1] row_mask:0xf bank_mask:0xf bound_ctrl:1
	s_nop 0
	v_cndmask_b32_e32 v38, v214, v38, vcc
	v_add_f32_dpp v29, v29, v29 row_half_mirror row_mask:0xf bank_mask:0xf bound_ctrl:1
	v_lshlrev_b32_e32 v46, 2, v38
	s_nop 0
	v_add_f32_dpp v29, v29, v29 row_mirror row_mask:0xf bank_mask:0xf bound_ctrl:1
	v_mov_b32_e32 v38, v29
	v_mov_b32_e32 v108, v29
	s_nop 1
	v_permlane16_swap_b32_e32 v38, v108
	v_add_f32_e32 v29, v38, v108
	v_xor_b32_e32 v38, 32, v214
	v_cmp_lt_i32_e32 vcc, v38, v39
	s_nop 1
	v_cndmask_b32_e32 v38, v214, v38, vcc
	v_lshlrev_b32_e32 v47, 2, v38
	v_mov_b32_e32 v38, v29
	v_mov_b32_e32 v108, v29
	s_nop 1
	v_permlane32_swap_b32_e32 v38, v108
	v_add_f32_e32 v29, v38, v108
	v_fmamk_f32 v31, v29, 0xbb000000, v31
	v_fmamk_f32 v30, v29, 0xbb000000, v30
	v_fmamk_f32 v33, v29, 0xbb000000, v33
	v_fmac_f32_e32 v32, 0xbb000000, v29
	v_pk_mul_f32 v[38:39], v[32:33], v[32:33]
	v_pk_mul_f32 v[40:41], v[30:31], v[30:31]
	v_fmamk_f32 v35, v29, 0xbb000000, v35
	v_fmamk_f32 v34, v29, 0xbb000000, v34
	v_fmamk_f32 v37, v29, 0xbb000000, v37
	v_fmac_f32_e32 v36, 0xbb000000, v29
	v_pk_mov_b32 v[42:43], v[40:41], v[38:39] op_sel:[1,0]
	v_mov_b32_e32 v41, v39
	v_pk_add_f32 v[38:39], v[42:43], v[40:41]
	v_pk_mul_f32 v[40:41], v[36:37], v[36:37]
	v_pk_mul_f32 v[42:43], v[34:35], v[34:35]
	v_mov_b32_e32 v44, v40
	v_mov_b32_e32 v45, v42
	v_mov_b32_e32 v42, v41
	v_pk_add_f32 v[40:41], v[44:45], v[42:43]
	v_add_f32_e32 v29, v38, v39
	v_add_f32_e32 v29, v41, v29
	v_add_f32_e32 v29, v40, v29
	s_nop 1
	v_add_f32_dpp v29, v29, v29 quad_perm:[1,0,3,2] row_mask:0xf bank_mask:0xf bound_ctrl:1
	s_nop 1
	v_add_f32_dpp v29, v29, v29 quad_perm:[2,3,0,1] row_mask:0xf bank_mask:0xf bound_ctrl:1
	s_nop 1
	v_add_f32_dpp v29, v29, v29 row_half_mirror row_mask:0xf bank_mask:0xf bound_ctrl:1
	s_nop 1
	v_add_f32_dpp v29, v29, v29 row_mirror row_mask:0xf bank_mask:0xf bound_ctrl:1
	v_mov_b32_e32 v38, v29
	v_mov_b32_e32 v108, v29
	s_nop 1
	v_permlane16_swap_b32_e32 v38, v108
	v_add_f32_e32 v29, v38, v108
	v_mov_b32_e32 v38, v29
	v_mov_b32_e32 v108, v29
	s_nop 1
	v_permlane32_swap_b32_e32 v38, v108
	v_add_f32_e32 v29, v38, v108
	v_fmamk_f32 v29, v29, 0x3b000000, v1
	v_mul_f32_e32 v38, 0x4b800000, v29
	v_cmp_gt_f32_e32 vcc, s77, v29
	s_nop 1
	v_cndmask_b32_e32 v29, v29, v38, vcc
	v_rsq_f32_e32 v29, v29
	s_nop 0
	v_mul_f32_e32 v38, 0x45800000, v29
	v_cndmask_b32_e32 v38, v29, v38, vcc
	v_pk_mul_f32 v[30:31], v[30:31], v[38:39] op_sel_hi:[1,0]
	v_pk_mul_f32 v[34:35], v[34:35], v[38:39] op_sel_hi:[1,0]
	v_pk_fma_f32 v[30:31], v[6:7], v[30:31], v[14:15]
	v_pk_fma_f32 v[34:35], v[2:3], v[34:35], v[10:11]
	v_mul_f32_e32 v29, 0xbfb8aa3b, v30
	v_pk_mul_f32 v[32:33], v[32:33], v[38:39] op_sel_hi:[1,0]
	v_pk_mul_f32 v[36:37], v[36:37], v[38:39] op_sel_hi:[1,0]
	v_exp_f32_e32 v29, v29
	v_mul_f32_e32 v38, 0xbfb8aa3b, v34
	v_exp_f32_e32 v39, v38
	v_mul_f32_e32 v40, 0xbfb8aa3b, v35
	v_add_f32_e32 v29, 1.0, v29
	v_rcp_f32_e32 v38, v29
	v_add_f32_e32 v29, 1.0, v39
	v_mul_f32_e32 v39, 0xbfb8aa3b, v31
	v_exp_f32_e32 v39, v39
	v_exp_f32_e32 v41, v40
	v_pk_fma_f32 v[32:33], v[8:9], v[32:33], v[16:17]
	v_rcp_f32_e32 v40, v29
	v_add_f32_e32 v29, 1.0, v39
	v_pk_fma_f32 v[36:37], v[4:5], v[36:37], v[12:13]
	v_rcp_f32_e32 v39, v29
	v_add_f32_e32 v29, 1.0, v41
	v_mul_f32_e32 v41, 0xbfb8aa3b, v32
	v_exp_f32_e32 v42, v41
	v_mul_f32_e32 v41, 0xbfb8aa3b, v36
	v_exp_f32_e32 v43, v41
	v_rcp_f32_e32 v41, v29
	v_add_f32_e32 v29, 1.0, v42
	v_rcp_f32_e32 v42, v29
	v_add_f32_e32 v29, 1.0, v43
	v_mul_f32_e32 v43, 0xbfb8aa3b, v33
	v_exp_f32_e32 v43, v43
	v_mul_f32_e32 v44, 0xbfb8aa3b, v37
	v_exp_f32_e32 v45, v44
	v_rcp_f32_e32 v44, v29
	v_add_f32_e32 v29, 1.0, v43
	v_rcp_f32_e32 v43, v29
	v_add_f32_e32 v29, 1.0, v45
	v_rcp_f32_e32 v45, v29
	v_pk_mul_f32 v[30:31], v[30:31], v[38:39]
	v_pk_mul_f32 v[34:35], v[34:35], v[40:41]
	v_pk_mul_f32 v[32:33], v[32:33], v[42:43]
	v_pk_mul_f32 v[36:37], v[36:37], v[44:45]
	v_cvt_pk_bf16_f32 v30, v30, v31
	v_cvt_pk_bf16_f32 v31, v32, v33
	v_cvt_pk_bf16_f32 v32, v34, v35
	v_cvt_pk_bf16_f32 v33, v36, v37
	global_store_dwordx4 v[20:21], v[30:33], off
	s_branch .LBB0_2164
